# SB tile: all eight K fragments and all sixteen V fragments requested in one LDS round trip each (section 7.1); P pack moved ahead of the preceding PV MFMA so the VALU-to-MFMA distance is two states
# speedup vs baseline: 1.0048x; 1.0016x over previous
.LBB0_538:
	s_and_b64 vcc, exec, s[4:5]
	s_mov_b64 s[4:5], -1
	s_cbranch_vccnz .LBB0_545
	s_cmp_gt_i32 s41, s37
	s_mov_b64 s[4:5], 0
	s_cbranch_scc1 .LBB0_545
	v_add_u32_e32 v3, s98, v185
	ds_read_b128 v[38:41], v3
	ds_read_b128 v[42:45], v3 offset:512
	ds_read_b128 v[86:89], v3 offset:2048
	ds_read_b128 v[90:93], v3 offset:2560
	ds_read_b128 v[216:219], v3 offset:4096
	ds_read_b128 v[220:223], v3 offset:4608
	ds_read_b128 v[224:227], v3 offset:6144
	ds_read_b128 v[228:231], v3 offset:6656
	s_add_i32 s18, s41, 63
	s_waitcnt lgkmcnt(7)
	v_mfma_f32_32x32x16_bf16 v[54:69], v[38:41], v[82:85], 0
	s_mov_b64 s[4:5], -1
	s_cmp_lt_i32 s18, s34
	s_waitcnt lgkmcnt(6)
	v_mfma_f32_32x32x16_bf16 v[38:53], v[42:45], v[82:85], 0
	s_waitcnt lgkmcnt(5)
	v_mfma_f32_32x32x16_bf16 v[54:69], v[86:89], v[78:81], v[54:69]
	s_waitcnt lgkmcnt(4)
	v_mfma_f32_32x32x16_bf16 v[38:53], v[90:93], v[78:81], v[38:53]
	s_waitcnt lgkmcnt(3)
	v_mfma_f32_32x32x16_bf16 v[54:69], v[216:219], v[74:77], v[54:69]
	s_waitcnt lgkmcnt(2)
	v_mfma_f32_32x32x16_bf16 v[38:53], v[220:223], v[74:77], v[38:53]
	s_waitcnt lgkmcnt(1)
	v_mfma_f32_32x32x16_bf16 v[54:69], v[224:227], v[70:73], v[54:69]
	s_waitcnt lgkmcnt(0)
	v_mfma_f32_32x32x16_bf16 v[38:53], v[228:231], v[70:73], v[38:53]
	s_nop 9
	v_exp_f32_e64 v247, -|v54|
	v_exp_f32_e64 v246, -|v55|
	v_exp_f32_e64 v239, -|v56|
	v_exp_f32_e64 v238, -|v57|
	v_exp_f32_e64 v231, -|v58|
	v_exp_f32_e64 v230, -|v59|
	v_exp_f32_e64 v223, -|v60|
	v_exp_f32_e64 v243, -|v38|
	v_exp_f32_e64 v242, -|v39|
	v_exp_f32_e64 v235, -|v40|
	v_exp_f32_e64 v234, -|v41|
	v_exp_f32_e64 v227, -|v42|
	v_exp_f32_e64 v226, -|v43|
	v_exp_f32_e64 v222, -|v61|
	v_exp_f32_e64 v219, -|v44|
	v_exp_f32_e64 v218, -|v45|
	v_exp_f32_e64 v215, -|v62|
	v_exp_f32_e64 v213, -|v63|
	v_exp_f32_e64 v211, -|v46|
	v_exp_f32_e64 v210, -|v47|
	v_exp_f32_e64 v207, -|v64|
	v_exp_f32_e64 v206, -|v65|
	v_exp_f32_e64 v203, -|v48|
	v_exp_f32_e64 v202, -|v49|
	v_exp_f32_e64 v199, -|v66|
	v_exp_f32_e64 v198, -|v67|
	v_exp_f32_e64 v195, -|v50|
	v_exp_f32_e64 v194, -|v51|
	v_exp_f32_e64 v190, -|v68|
	v_exp_f32_e64 v189, -|v69|
	v_exp_f32_e64 v187, -|v52|
	v_exp_f32_e64 v186, -|v53|
	s_cbranch_scc1 .LBB0_542
	v_add_f32_e32 v86, 1.0, v247
	v_add_f32_e32 v87, 1.0, v246
	v_log_f32_e32 v86, v86
	v_log_f32_e32 v87, v87
	v_max_f32_e32 v88, 0, v54
	v_max_f32_e32 v89, 0, v55
	v_cmp_lt_i32_e32 vcc, 0, v184
	v_pk_add_f32 v[86:87], v[88:89], v[86:87]
	v_cmp_lt_i32_e64 s[4:5], 1, v184
	v_pk_add_f32 v[88:89], v[54:55], v[86:87] neg_lo:[0,1] neg_hi:[0,1]
	v_cndmask_b32_e32 v86, 0, v86, vcc
	v_cndmask_b32_e64 v87, 0, v87, s[4:5]
	v_and_b32_e32 v91, 0xffff0000, v87
	v_and_b32_e32 v90, 0xffff0000, v86
	v_cndmask_b32_e32 v124, v161, v88, vcc
	v_cndmask_b32_e64 v125, v161, v89, s[4:5]
	v_pk_add_f32 v[88:89], v[86:87], 0 op_sel_hi:[1,0]
	v_or_b32_sdwa v98, v91, v86 dst_sel:DWORD dst_unused:UNUSED_PAD src0_sel:DWORD src1_sel:WORD_1
	v_pk_add_f32 v[86:87], v[86:87], v[90:91] neg_lo:[0,1] neg_hi:[0,1]
	v_add_f32_e32 v90, 1.0, v243
	v_add_f32_e32 v91, 1.0, v242
	v_log_f32_e32 v90, v90
	v_log_f32_e32 v91, v91
	v_cvt_pk_bf16_f32 v94, v86, v87
	v_max_f32_e32 v86, 0, v38
	v_max_f32_e32 v87, 0, v39
	v_pk_add_f32 v[86:87], v[86:87], v[90:91]
	v_cmp_lt_i32_e32 vcc, 32, v184
	v_pk_add_f32 v[90:91], v[38:39], v[86:87] neg_lo:[0,1] neg_hi:[0,1]
	v_cmp_lt_i32_e64 s[4:5], 33, v184
	v_cndmask_b32_e32 v126, v161, v90, vcc
	v_cndmask_b32_e32 v90, 0, v86, vcc
	v_cndmask_b32_e64 v127, v161, v91, s[4:5]
	v_cndmask_b32_e64 v91, 0, v87, s[4:5]
	v_and_b32_e32 v93, 0xffff0000, v91
	v_and_b32_e32 v92, 0xffff0000, v90
	v_add_f32_e32 v87, 1.0, v239
	v_pk_add_f32 v[88:89], v[90:91], v[88:89]
	v_or_b32_sdwa v86, v93, v90 dst_sel:DWORD dst_unused:UNUSED_PAD src0_sel:DWORD src1_sel:WORD_1
	v_pk_add_f32 v[90:91], v[90:91], v[92:93] neg_lo:[0,1] neg_hi:[0,1]
	v_log_f32_e32 v92, v87
	v_add_f32_e32 v87, 1.0, v238
	v_log_f32_e32 v93, v87
	v_max_f32_e32 v96, 0, v56
	v_max_f32_e32 v97, 0, v57
	v_cmp_lt_i32_e32 vcc, 2, v184
	v_pk_add_f32 v[92:93], v[96:97], v[92:93]
	v_cmp_lt_i32_e64 s[4:5], 3, v184
	v_pk_add_f32 v[96:97], v[56:57], v[92:93] neg_lo:[0,1] neg_hi:[0,1]
	v_cndmask_b32_e32 v92, 0, v92, vcc
	v_cndmask_b32_e64 v93, 0, v93, s[4:5]
	v_cndmask_b32_e32 v128, v161, v96, vcc
	v_cndmask_b32_e64 v129, v161, v97, s[4:5]
	v_and_b32_e32 v97, 0xffff0000, v93
	v_and_b32_e32 v96, 0xffff0000, v92
	v_add_f32_e32 v87, 1.0, v235
	v_pk_add_f32 v[88:89], v[92:93], v[88:89]
	v_or_b32_sdwa v99, v97, v92 dst_sel:DWORD dst_unused:UNUSED_PAD src0_sel:DWORD src1_sel:WORD_1
	v_pk_add_f32 v[92:93], v[92:93], v[96:97] neg_lo:[0,1] neg_hi:[0,1]
	v_log_f32_e32 v96, v87
	v_add_f32_e32 v87, 1.0, v234
	v_log_f32_e32 v97, v87
	v_cvt_pk_bf16_f32 v95, v92, v93
	v_max_f32_e32 v92, 0, v40
	v_max_f32_e32 v93, 0, v41
	v_pk_add_f32 v[92:93], v[92:93], v[96:97]
	v_cmp_lt_i32_e32 vcc, 34, v184
	v_cmp_lt_i32_e64 s[4:5], 35, v184
	v_pk_add_f32 v[96:97], v[40:41], v[92:93] neg_lo:[0,1] neg_hi:[0,1]
	v_cndmask_b32_e32 v92, 0, v92, vcc
	v_cndmask_b32_e64 v93, 0, v93, s[4:5]
	v_cvt_pk_bf16_f32 v90, v90, v91
	v_cndmask_b32_e32 v130, v161, v96, vcc
	v_cndmask_b32_e64 v131, v161, v97, s[4:5]
	v_and_b32_e32 v97, 0xffff0000, v93
	v_and_b32_e32 v96, 0xffff0000, v92
	v_add_f32_e32 v91, 1.0, v231
	v_pk_add_f32 v[88:89], v[92:93], v[88:89]
	v_or_b32_sdwa v87, v97, v92 dst_sel:DWORD dst_unused:UNUSED_PAD src0_sel:DWORD src1_sel:WORD_1
	v_pk_add_f32 v[92:93], v[92:93], v[96:97] neg_lo:[0,1] neg_hi:[0,1]
	v_log_f32_e32 v96, v91
	v_add_f32_e32 v91, 1.0, v230
	v_log_f32_e32 v97, v91
	v_cvt_pk_bf16_f32 v91, v92, v93
	v_max_f32_e32 v92, 0, v58
	v_max_f32_e32 v93, 0, v59
	v_pk_add_f32 v[92:93], v[92:93], v[96:97]
	v_cmp_lt_i32_e32 vcc, 8, v184
	v_cmp_lt_i32_e64 s[4:5], 9, v184
	v_pk_add_f32 v[96:97], v[58:59], v[92:93] neg_lo:[0,1] neg_hi:[0,1]
	v_cndmask_b32_e32 v92, 0, v92, vcc
	v_cndmask_b32_e64 v93, 0, v93, s[4:5]
	v_cndmask_b32_e32 v132, v161, v96, vcc
	v_cndmask_b32_e64 v133, v161, v97, s[4:5]
	v_and_b32_e32 v97, 0xffff0000, v93
	v_and_b32_e32 v96, 0xffff0000, v92
	v_pk_add_f32 v[88:89], v[92:93], v[88:89]
	v_or_b32_sdwa v100, v97, v92 dst_sel:DWORD dst_unused:UNUSED_PAD src0_sel:DWORD src1_sel:WORD_1
	v_pk_add_f32 v[92:93], v[92:93], v[96:97] neg_lo:[0,1] neg_hi:[0,1]
	v_add_f32_e32 v96, 1.0, v227
	v_log_f32_e32 v102, v96
	v_add_f32_e32 v96, 1.0, v226
	v_log_f32_e32 v103, v96
	v_cvt_pk_bf16_f32 v96, v92, v93
	v_max_f32_e32 v92, 0, v42
	v_max_f32_e32 v93, 0, v43
	v_pk_add_f32 v[92:93], v[92:93], v[102:103]
	v_cmp_lt_i32_e32 vcc, 40, v184
	v_cmp_lt_i32_e64 s[4:5], 41, v184
	v_pk_add_f32 v[102:103], v[42:43], v[92:93] neg_lo:[0,1] neg_hi:[0,1]
	v_cndmask_b32_e32 v92, 0, v92, vcc
	v_cndmask_b32_e64 v93, 0, v93, s[4:5]
	v_cndmask_b32_e32 v134, v161, v102, vcc
	v_cndmask_b32_e64 v135, v161, v103, s[4:5]
	v_pk_add_f32 v[102:103], v[92:93], v[88:89]
	v_and_b32_e32 v105, 0xffff0000, v93
	v_and_b32_e32 v104, 0xffff0000, v92
	v_add_f32_e32 v89, 1.0, v223
	v_or_b32_sdwa v88, v105, v92 dst_sel:DWORD dst_unused:UNUSED_PAD src0_sel:DWORD src1_sel:WORD_1
	v_pk_add_f32 v[92:93], v[92:93], v[104:105] neg_lo:[0,1] neg_hi:[0,1]
	v_log_f32_e32 v104, v89
	v_add_f32_e32 v89, 1.0, v222
	v_log_f32_e32 v105, v89
	v_max_f32_e32 v106, 0, v60
	v_max_f32_e32 v107, 0, v61
	v_cmp_lt_i32_e32 vcc, 10, v184
	v_pk_add_f32 v[104:105], v[106:107], v[104:105]
	v_cmp_lt_i32_e64 s[4:5], 11, v184
	v_pk_add_f32 v[106:107], v[60:61], v[104:105] neg_lo:[0,1] neg_hi:[0,1]
	v_cndmask_b32_e32 v104, 0, v104, vcc
	v_cndmask_b32_e64 v105, 0, v105, s[4:5]
	v_cndmask_b32_e32 v136, v161, v106, vcc
	v_cndmask_b32_e64 v137, v161, v107, s[4:5]
	v_and_b32_e32 v107, 0xffff0000, v105
	v_and_b32_e32 v106, 0xffff0000, v104
	v_add_f32_e32 v89, 1.0, v219
	v_pk_add_f32 v[102:103], v[104:105], v[102:103]
	v_or_b32_sdwa v101, v107, v104 dst_sel:DWORD dst_unused:UNUSED_PAD src0_sel:DWORD src1_sel:WORD_1
	v_pk_add_f32 v[104:105], v[104:105], v[106:107] neg_lo:[0,1] neg_hi:[0,1]
	v_log_f32_e32 v106, v89
	v_add_f32_e32 v89, 1.0, v218
	v_log_f32_e32 v107, v89
	v_cvt_pk_bf16_f32 v97, v104, v105
	v_max_f32_e32 v104, 0, v44
	v_max_f32_e32 v105, 0, v45
	v_pk_add_f32 v[104:105], v[104:105], v[106:107]
	v_cmp_lt_i32_e32 vcc, 42, v184
	v_cmp_lt_i32_e64 s[4:5], 43, v184
	v_pk_add_f32 v[106:107], v[44:45], v[104:105] neg_lo:[0,1] neg_hi:[0,1]
	v_cndmask_b32_e32 v104, 0, v104, vcc
	v_cndmask_b32_e64 v105, 0, v105, s[4:5]
	v_cvt_pk_bf16_f32 v92, v92, v93
	v_cndmask_b32_e32 v138, v161, v106, vcc
	v_cndmask_b32_e64 v139, v161, v107, s[4:5]
	v_and_b32_e32 v107, 0xffff0000, v105
	v_and_b32_e32 v106, 0xffff0000, v104
	v_add_f32_e32 v93, 1.0, v215
	v_pk_add_f32 v[102:103], v[104:105], v[102:103]
	v_or_b32_sdwa v89, v107, v104 dst_sel:DWORD dst_unused:UNUSED_PAD src0_sel:DWORD src1_sel:WORD_1
	v_pk_add_f32 v[104:105], v[104:105], v[106:107] neg_lo:[0,1] neg_hi:[0,1]
	v_log_f32_e32 v106, v93
	v_add_f32_e32 v93, 1.0, v213
	v_log_f32_e32 v107, v93
	v_cvt_pk_bf16_f32 v93, v104, v105
	v_max_f32_e32 v104, 0, v62
	v_max_f32_e32 v105, 0, v63
	v_pk_add_f32 v[104:105], v[104:105], v[106:107]
	v_cmp_lt_i32_e32 vcc, 16, v184
	v_cmp_lt_i32_e64 s[4:5], 17, v184
	v_pk_add_f32 v[106:107], v[62:63], v[104:105] neg_lo:[0,1] neg_hi:[0,1]
	v_cndmask_b32_e32 v104, 0, v104, vcc
	v_cndmask_b32_e64 v105, 0, v105, s[4:5]
	v_cndmask_b32_e32 v140, v161, v106, vcc
	v_cndmask_b32_e64 v141, v161, v107, s[4:5]
	v_and_b32_e32 v107, 0xffff0000, v105
	v_and_b32_e32 v106, 0xffff0000, v104
	v_pk_add_f32 v[102:103], v[104:105], v[102:103]
	v_or_b32_sdwa v110, v107, v104 dst_sel:DWORD dst_unused:UNUSED_PAD src0_sel:DWORD src1_sel:WORD_1
	v_pk_add_f32 v[104:105], v[104:105], v[106:107] neg_lo:[0,1] neg_hi:[0,1]
	v_add_f32_e32 v106, 1.0, v211
	v_add_f32_e32 v107, 1.0, v210
	v_log_f32_e32 v106, v106
	v_log_f32_e32 v107, v107
	v_cvt_pk_bf16_f32 v114, v104, v105
	v_max_f32_e32 v104, 0, v46
	v_max_f32_e32 v105, 0, v47
	v_pk_add_f32 v[104:105], v[104:105], v[106:107]
	v_cmp_lt_i32_e32 vcc, 48, v184
	v_cmp_lt_i32_e64 s[4:5], 49, v184
	v_pk_add_f32 v[106:107], v[46:47], v[104:105] neg_lo:[0,1] neg_hi:[0,1]
	v_cndmask_b32_e32 v104, 0, v104, vcc
	v_cndmask_b32_e64 v105, 0, v105, s[4:5]
	v_pk_add_f32 v[108:109], v[104:105], v[102:103]
	v_and_b32_e32 v103, 0xffff0000, v105
	v_and_b32_e32 v102, 0xffff0000, v104
	v_cndmask_b32_e32 v144, v161, v106, vcc
	v_or_b32_sdwa v106, v103, v104 dst_sel:DWORD dst_unused:UNUSED_PAD src0_sel:DWORD src1_sel:WORD_1
	v_pk_add_f32 v[102:103], v[104:105], v[102:103] neg_lo:[0,1] neg_hi:[0,1]
	v_add_f32_e32 v104, 1.0, v207
	v_add_f32_e32 v105, 1.0, v206
	v_log_f32_e32 v104, v104
	v_log_f32_e32 v105, v105
	v_max_f32_e32 v112, 0, v64
	v_max_f32_e32 v113, 0, v65
	v_cndmask_b32_e64 v145, v161, v107, s[4:5]
	v_pk_add_f32 v[104:105], v[112:113], v[104:105]
	v_cmp_lt_i32_e32 vcc, 18, v184
	v_cmp_lt_i32_e64 s[4:5], 19, v184
	v_pk_add_f32 v[112:113], v[64:65], v[104:105] neg_lo:[0,1] neg_hi:[0,1]
	v_cndmask_b32_e32 v104, 0, v104, vcc
	v_cndmask_b32_e64 v105, 0, v105, s[4:5]
	v_cvt_pk_bf16_f32 v102, v102, v103
	v_cndmask_b32_e32 v146, v161, v112, vcc
	v_cndmask_b32_e64 v147, v161, v113, s[4:5]
	v_and_b32_e32 v113, 0xffff0000, v105
	v_and_b32_e32 v112, 0xffff0000, v104
	v_add_f32_e32 v103, 1.0, v203
	v_pk_add_f32 v[108:109], v[104:105], v[108:109]
	v_or_b32_sdwa v111, v113, v104 dst_sel:DWORD dst_unused:UNUSED_PAD src0_sel:DWORD src1_sel:WORD_1
	v_pk_add_f32 v[104:105], v[104:105], v[112:113] neg_lo:[0,1] neg_hi:[0,1]
	v_log_f32_e32 v112, v103
	v_add_f32_e32 v103, 1.0, v202
	v_log_f32_e32 v113, v103
	v_cvt_pk_bf16_f32 v115, v104, v105
	v_max_f32_e32 v104, 0, v48
	v_max_f32_e32 v105, 0, v49
	v_pk_add_f32 v[104:105], v[104:105], v[112:113]
	v_cmp_lt_i32_e32 vcc, 50, v184
	v_cmp_lt_i32_e64 s[4:5], 51, v184
	v_pk_add_f32 v[112:113], v[48:49], v[104:105] neg_lo:[0,1] neg_hi:[0,1]
	v_cndmask_b32_e32 v104, 0, v104, vcc
	v_cndmask_b32_e64 v105, 0, v105, s[4:5]
	v_cndmask_b32_e32 v152, v161, v112, vcc
	v_cndmask_b32_e64 v153, v161, v113, s[4:5]
	v_and_b32_e32 v113, 0xffff0000, v105
	v_and_b32_e32 v112, 0xffff0000, v104
	v_add_f32_e32 v103, 1.0, v199
	v_pk_add_f32 v[108:109], v[104:105], v[108:109]
	v_or_b32_sdwa v107, v113, v104 dst_sel:DWORD dst_unused:UNUSED_PAD src0_sel:DWORD src1_sel:WORD_1
	v_pk_add_f32 v[104:105], v[104:105], v[112:113] neg_lo:[0,1] neg_hi:[0,1]
	v_log_f32_e32 v112, v103
	v_add_f32_e32 v103, 1.0, v198
	v_log_f32_e32 v113, v103
	v_cvt_pk_bf16_f32 v103, v104, v105
	v_max_f32_e32 v104, 0, v66
	v_max_f32_e32 v105, 0, v67
	v_pk_add_f32 v[104:105], v[104:105], v[112:113]
	v_cmp_lt_i32_e64 s[4:5], 25, v184
	v_pk_add_f32 v[112:113], v[66:67], v[104:105] neg_lo:[0,1] neg_hi:[0,1]
	v_cmp_lt_i32_e32 vcc, 24, v184
	v_cndmask_b32_e64 v157, v161, v113, s[4:5]
	v_add_f32_e32 v113, 1.0, v195
	v_log_f32_e32 v142, v113
	v_add_f32_e32 v113, 1.0, v194
	v_cndmask_b32_e64 v105, 0, v105, s[4:5]
	v_cndmask_b32_e32 v104, 0, v104, vcc
	v_log_f32_e32 v143, v113
	v_and_b32_e32 v117, 0xffff0000, v105
	v_and_b32_e32 v116, 0xffff0000, v104
	v_cndmask_b32_e32 v156, v161, v112, vcc
	v_pk_add_f32 v[108:109], v[104:105], v[108:109]
	v_or_b32_sdwa v112, v117, v104 dst_sel:DWORD dst_unused:UNUSED_PAD src0_sel:DWORD src1_sel:WORD_1
	v_pk_add_f32 v[104:105], v[104:105], v[116:117] neg_lo:[0,1] neg_hi:[0,1]
	v_cmp_lt_i32_e32 vcc, 56, v184
	v_cvt_pk_bf16_f32 v116, v104, v105
	v_max_f32_e32 v104, 0, v50
	v_max_f32_e32 v105, 0, v51
	v_pk_add_f32 v[104:105], v[104:105], v[142:143]
	v_cmp_lt_i32_e64 s[4:5], 57, v184
	v_pk_add_f32 v[142:143], v[50:51], v[104:105] neg_lo:[0,1] neg_hi:[0,1]
	v_cndmask_b32_e32 v104, 0, v104, vcc
	v_cndmask_b32_e64 v105, 0, v105, s[4:5]
	v_cndmask_b32_e32 v158, v161, v142, vcc
	v_cndmask_b32_e64 v159, v161, v143, s[4:5]
	v_pk_add_f32 v[142:143], v[104:105], v[108:109]
	v_and_b32_e32 v149, 0xffff0000, v105
	v_and_b32_e32 v148, 0xffff0000, v104
	v_add_f32_e32 v109, 1.0, v190
	v_or_b32_sdwa v108, v149, v104 dst_sel:DWORD dst_unused:UNUSED_PAD src0_sel:DWORD src1_sel:WORD_1
	v_pk_add_f32 v[104:105], v[104:105], v[148:149] neg_lo:[0,1] neg_hi:[0,1]
	v_log_f32_e32 v148, v109
	v_add_f32_e32 v109, 1.0, v189
	v_log_f32_e32 v149, v109
	v_max_f32_e32 v150, 0, v68
	v_max_f32_e32 v151, 0, v69
	v_cmp_lt_i32_e32 vcc, 26, v184
	v_pk_add_f32 v[148:149], v[150:151], v[148:149]
	v_cmp_lt_i32_e64 s[4:5], 27, v184
	v_pk_add_f32 v[150:151], v[68:69], v[148:149] neg_lo:[0,1] neg_hi:[0,1]
	v_cndmask_b32_e32 v148, 0, v148, vcc
	v_cndmask_b32_e64 v149, 0, v149, s[4:5]
	v_cvt_pk_bf16_f32 v104, v104, v105
	v_cndmask_b32_e32 v154, v161, v150, vcc
	v_cndmask_b32_e64 v155, v161, v151, s[4:5]
	v_and_b32_e32 v151, 0xffff0000, v149
	v_and_b32_e32 v150, 0xffff0000, v148
	v_add_f32_e32 v105, 1.0, v187
	v_pk_add_f32 v[142:143], v[148:149], v[142:143]
	v_or_b32_sdwa v113, v151, v148 dst_sel:DWORD dst_unused:UNUSED_PAD src0_sel:DWORD src1_sel:WORD_1
	v_pk_add_f32 v[148:149], v[148:149], v[150:151] neg_lo:[0,1] neg_hi:[0,1]
	v_log_f32_e32 v150, v105
	v_add_f32_e32 v105, 1.0, v186
	v_log_f32_e32 v151, v105
	v_cvt_pk_bf16_f32 v117, v148, v149
	v_max_f32_e32 v148, 0, v52
	v_max_f32_e32 v149, 0, v53
	v_pk_add_f32 v[148:149], v[148:149], v[150:151]
	v_cmp_lt_i32_e32 vcc, 58, v184
	v_pk_add_f32 v[150:151], v[52:53], v[148:149] neg_lo:[0,1] neg_hi:[0,1]
	v_cmp_lt_i32_e64 s[4:5], 59, v184
	v_cndmask_b32_e32 v150, v161, v150, vcc
	v_cndmask_b32_e32 v148, 0, v148, vcc
	v_cndmask_b32_e64 v151, v161, v151, s[4:5]
	v_cndmask_b32_e64 v149, 0, v149, s[4:5]
	s_mov_b64 s[4:5], 0

.LBB0_544:
	s_mov_b32 s4, 0x43000000
	v_mov_b32_e32 v37, v36
	v_mov_b32_e32 v38, v36
	v_mov_b32_e32 v39, v36
	v_mov_b32_e32 v40, v36
	v_mov_b32_e32 v41, v36
	v_mov_b32_e32 v42, v36
	v_mov_b32_e32 v43, v36
	v_mov_b32_e32 v44, v36
	v_mov_b32_e32 v45, v36
	v_mov_b32_e32 v46, v36
	v_mov_b32_e32 v47, v36
	v_mov_b32_e32 v48, v36
	v_mov_b32_e32 v49, v36
	v_mov_b32_e32 v50, v36
	v_mov_b32_e32 v51, v36
	v_and_b32_e32 v53, 0xffff0000, v149
	v_and_b32_e32 v52, 0xffff0000, v148
	v_add_u32_e32 v3, s98, v167
	ds_read_b64_tr_b16 v[216:217], v3
	ds_read_b64_tr_b16 v[218:219], v3 offset:512
	ds_read_b64_tr_b16 v[220:221], v3 offset:4096
	ds_read_b64_tr_b16 v[222:223], v3 offset:4608
	ds_read_b64_tr_b16 v[224:225], v3 offset:1024
	ds_read_b64_tr_b16 v[226:227], v3 offset:1536
	ds_read_b64_tr_b16 v[228:229], v3 offset:5120
	ds_read_b64_tr_b16 v[230:231], v3 offset:5632
	ds_read_b64_tr_b16 v[232:233], v3 offset:2048
	ds_read_b64_tr_b16 v[234:235], v3 offset:2560
	ds_read_b64_tr_b16 v[236:237], v3 offset:6144
	ds_read_b64_tr_b16 v[238:239], v3 offset:6656
	ds_read_b64_tr_b16 v[240:241], v3 offset:3072
	ds_read_b64_tr_b16 v[242:243], v3 offset:3584
	ds_read_b64_tr_b16 v[244:245], v3 offset:7168
	ds_read_b64_tr_b16 v[246:247], v3 offset:7680
	v_mfma_f32_32x32x16_bf16 v[54:69], v[172:175], v[98:101], v[36:51]
	v_or_b32_sdwa v109, v53, v148 dst_sel:DWORD dst_unused:UNUSED_PAD src0_sel:DWORD src1_sel:WORD_1
	v_add_f32_e64 v52, v148, -v52
	v_add_f32_e64 v53, v149, -v53
	v_mfma_f32_32x32x16_bf16 v[200:215], v[172:175], v[86:89], v[36:51]
	v_cvt_pk_bf16_f32 v105, v52, v53
	v_mfma_f32_32x32x16_bf16 v[54:69], v[172:175], v[94:97], v[54:69]
	v_mfma_f32_32x32x16_bf16 v[200:215], v[172:175], v[90:93], v[200:215]
	v_mfma_f32_32x32x16_bf16 v[54:69], v[176:179], v[110:113], v[54:69]
	v_mfma_f32_32x32x16_bf16 v[54:69], v[176:179], v[114:117], v[54:69]
	v_mfma_f32_32x32x16_bf16 v[54:69], v[180:183], v[86:89], v[54:69]
	v_mfma_f32_32x32x16_bf16 v[200:215], v[176:179], v[106:109], v[200:215]
	v_mfma_f32_32x32x16_bf16 v[54:69], v[180:183], v[90:93], v[54:69]
	v_mfma_f32_32x32x16_bf16 v[54:69], v[180:183], v[106:109], v[54:69]
	v_mfma_f32_32x32x16_bf16 v[200:215], v[176:179], v[102:105], v[200:215]
	v_mfma_f32_32x32x16_bf16 v[54:69], v[180:183], v[102:105], v[54:69]
	s_nop 10
	v_sub_f32_e32 v38, v126, v200
	v_exp_f32_e32 v100, v38
	v_sub_f32_e32 v38, v125, v55
	v_exp_f32_e32 v55, v38
	v_sub_f32_e32 v38, v127, v201
	v_exp_f32_e32 v101, v38
	v_sub_f32_e32 v38, v128, v56
	v_exp_f32_e32 v56, v38
	v_sub_f32_e32 v38, v130, v202
	v_exp_f32_e32 v102, v38
	v_sub_f32_e32 v38, v129, v57
	v_exp_f32_e32 v57, v38
	v_sub_f32_e32 v38, v131, v203
	v_exp_f32_e32 v103, v38
	v_sub_f32_e32 v38, v132, v58
	v_exp_f32_e32 v58, v38
	v_sub_f32_e32 v38, v134, v204
	v_exp_f32_e32 v104, v38
	v_sub_f32_e32 v38, v133, v59
	v_exp_f32_e32 v59, v38
	v_sub_f32_e32 v38, v135, v205
	v_exp_f32_e32 v105, v38
	v_sub_f32_e32 v38, v136, v60
	v_exp_f32_e32 v60, v38
	v_sub_f32_e32 v38, v138, v206
	v_exp_f32_e32 v106, v38
	v_sub_f32_e32 v38, v137, v61
	v_exp_f32_e32 v61, v38
	v_sub_f32_e32 v38, v139, v207
	v_exp_f32_e32 v107, v38
	v_sub_f32_e32 v38, v140, v62
	v_exp_f32_e32 v62, v38
	v_sub_f32_e32 v38, v144, v208
	v_exp_f32_e32 v108, v38
	v_sub_f32_e32 v38, v141, v63
	v_exp_f32_e32 v63, v38
	v_sub_f32_e32 v38, v145, v209
	v_exp_f32_e32 v109, v38
	v_sub_f32_e32 v38, v146, v64
	v_exp_f32_e32 v64, v38
	v_sub_f32_e32 v38, v152, v210
	v_exp_f32_e32 v110, v38
	v_sub_f32_e32 v38, v147, v65
	v_exp_f32_e32 v65, v38
	v_sub_f32_e32 v38, v153, v211
	v_exp_f32_e32 v111, v38
	v_sub_f32_e32 v38, v156, v66
	v_exp_f32_e32 v66, v38
	v_sub_f32_e32 v38, v158, v212
	v_exp_f32_e32 v112, v38
	v_sub_f32_e32 v38, v157, v67
	v_exp_f32_e32 v50, v38
	v_sub_f32_e32 v38, v159, v213
	v_exp_f32_e32 v67, v38
	v_sub_f32_e32 v38, v154, v68
	v_sub_f32_e32 v54, v124, v54
	v_exp_f32_e32 v51, v38
	v_exp_f32_e32 v54, v54
	v_cvt_pk_bf16_f32 v43, v56, v57
	v_cvt_pk_bf16_f32 v42, v54, v55
	v_cvt_pk_bf16_f32 v44, v58, v59
	v_cvt_pk_bf16_f32 v45, v60, v61
	s_waitcnt lgkmcnt(14)
	s_nop 0
	v_mfma_f32_32x32x16_bf16 v[20:35], v[216:219], v[42:45], v[20:35]
	v_sub_f32_e32 v38, v155, v69
	v_exp_f32_e32 v41, v38
	v_cvt_pk_bf16_f32 v38, v62, v63
	v_cvt_pk_bf16_f32 v39, v64, v65
	v_cvt_pk_bf16_f32 v40, v66, v50
	v_cvt_pk_bf16_f32 v41, v51, v41
	s_waitcnt lgkmcnt(12)
	v_mfma_f32_32x32x16_bf16 v[4:19], v[220:223], v[42:45], v[4:19]
	s_waitcnt lgkmcnt(10)
	v_mfma_f32_32x32x16_bf16 v[20:35], v[224:227], v[38:41], v[20:35]
	v_sub_f32_e32 v46, v150, v214
	v_exp_f32_e32 v58, v46
	v_cvt_pk_bf16_f32 v46, v100, v101
	v_cvt_pk_bf16_f32 v47, v102, v103
	v_cvt_pk_bf16_f32 v48, v104, v105
	v_cvt_pk_bf16_f32 v49, v106, v107
	s_waitcnt lgkmcnt(8)
	v_mfma_f32_32x32x16_bf16 v[4:19], v[228:231], v[38:41], v[4:19]
	v_sub_f32_e32 v42, v151, v215
	v_exp_f32_e32 v45, v42
	s_waitcnt lgkmcnt(6)
	v_mfma_f32_32x32x16_bf16 v[20:35], v[232:235], v[46:49], v[20:35]
	v_cvt_pk_bf16_f32 v42, v108, v109
	v_cvt_pk_bf16_f32 v43, v110, v111
	v_cvt_pk_bf16_f32 v44, v112, v67
	v_cvt_pk_bf16_f32 v45, v58, v45
	s_waitcnt lgkmcnt(4)
	v_mfma_f32_32x32x16_bf16 v[4:19], v[236:239], v[46:49], v[4:19]
	v_add_f32_e64 v46, v148, v142
	v_add_f32_e64 v47, v149, v143
	v_pk_add_f32 v[46:47], v[46:47], v[46:47] op_sel:[0,1] op_sel_hi:[1,0]
	s_nop 0
	v_mov_b32_e32 v3, v46
	s_nop 1
	v_permlane32_swap_b32_e32 v46, v3
	s_waitcnt lgkmcnt(2)
	v_mfma_f32_32x32x16_bf16 v[20:35], v[240:243], v[42:45], v[20:35]
	v_add_f32_e32 v3, v46, v3
	v_add_f32_e32 v36, v36, v3
	v_cmp_lt_f32_e32 vcc, s4, v36
	s_cmp_eq_u64 vcc, exec
	s_cselect_b64 s[4:5], -1, 0
	s_waitcnt lgkmcnt(0)
	v_mfma_f32_32x32x16_bf16 v[4:19], v[244:247], v[42:45], v[4:19]
